# grid barrier variant: baseline two-level release (members wait for their XCD leader's generation word, published after the leader's agent-scope invalidate) but members then invalidate only their L1 (b
# speedup vs baseline: 1.0042x; 1.0010x over previous
.LBB0_138:
	s_or_b64 exec, exec, s[6:7]
	s_waitcnt vmcnt(0)
	buffer_inv sc0
	s_waitcnt vmcnt(0)
